# speedup vs baseline: 1.0084x; 1.0084x over previous
.LBB3_4:
	s_or_b64 exec, exec, s[34:35]
	v_add_u32_e32 v51, 16, v51
	v_cmp_ge_i32_e64 s[2:3], v51, v48
	s_or_b64 s[30:31], s[2:3], s[30:31]
	v_add_u32_e32 v59, -16, v59
	s_andn2_b64 exec, exec, s[30:31]
	s_cbranch_execz .LBB3_11
	.p2align	6

.LBB4_4:
	s_or_b64 exec, exec, s[4:5]
	ds_read2_b32 v[0:1], v31 offset1:4
	ds_read2_b32 v[2:3], v31 offset0:8 offset1:12
	v_min_i32_e32 v4, 16, v35
	v_cmp_gt_i32_e64 s[4:5], v35, v16
	v_cmp_lt_i32_e64 s[6:7], v32, v4
	s_waitcnt lgkmcnt(1)
	v_lshl_or_b32 v0, v0, 6, v29
	v_lshl_or_b32 v1, v1, 6, v29
	v_cndmask_b32_e64 v0, v36, v0, s[4:5]
	v_cndmask_b32_e64 v1, v36, v1, s[6:7]
	buffer_load_dwordx4 v[42:45], v0, s[12:15], 0 offen
	buffer_load_dwordx4 v[46:49], v1, s[12:15], 0 offen
	s_waitcnt lgkmcnt(0)
	v_lshl_or_b32 v0, v2, 6, v29
	v_cmp_lt_i32_e64 s[8:9], v33, v4
	v_cmp_lt_i32_e64 s[2:3], v34, v4
	v_mov_b32_e32 v54, 0
	v_cndmask_b32_e64 v40, v36, v0, s[8:9]
	v_lshl_or_b32 v0, v3, 6, v29
	v_cndmask_b32_e64 v4, v36, v0, s[2:3]
	buffer_load_dwordx4 v[50:53], v40, s[12:15], 0 offen
	buffer_load_dwordx4 v[0:3], v4, s[12:15], 0 offen
	v_mov_b32_e32 v4, 0
	v_mov_b32_e32 v40, 0
	v_mov_b32_e32 v55, 0
	v_add_u32_e32 v24, 16, v24
	v_add_u32_e32 v35, -16, v35
	s_waitcnt vmcnt(3)
	v_dot2c_f32_f16_e32 v4, v42, v6
	s_waitcnt vmcnt(2)
	v_dot2c_f32_f16_e32 v40, v46, v6
	v_dot2c_f32_f16_e32 v4, v43, v7
	v_dot2c_f32_f16_e32 v40, v47, v7
	v_dot2c_f32_f16_e32 v4, v44, v8
	v_dot2c_f32_f16_e32 v40, v48, v8
	v_dot2c_f32_f16_e32 v4, v45, v9
	v_dot2c_f32_f16_e32 v40, v49, v9
	s_waitcnt vmcnt(1)
	v_dot2c_f32_f16_e32 v54, v50, v6
	s_waitcnt vmcnt(0)
	v_dot2c_f32_f16_e32 v55, v0, v6
	v_dot2c_f32_f16_e32 v54, v51, v7
	v_dot2c_f32_f16_e32 v55, v1, v7
	v_dot2c_f32_f16_e32 v54, v52, v8
	v_dot2c_f32_f16_e32 v55, v2, v8
	v_dot2c_f32_f16_e32 v54, v53, v9
	v_add_f32_dpp v4, v4, v4 quad_perm:[1,0,3,2] row_mask:0xf bank_mask:0xf bound_ctrl:1
	v_dot2c_f32_f16_e32 v55, v3, v9
	v_add_f32_dpp v40, v40, v40 quad_perm:[1,0,3,2] row_mask:0xf bank_mask:0xf bound_ctrl:1
	v_add_f32_dpp v54, v54, v54 quad_perm:[1,0,3,2] row_mask:0xf bank_mask:0xf bound_ctrl:1
	v_add_f32_dpp v4, v4, v4 quad_perm:[2,3,0,1] row_mask:0xf bank_mask:0xf bound_ctrl:1
	v_add_f32_dpp v55, v55, v55 quad_perm:[1,0,3,2] row_mask:0xf bank_mask:0xf bound_ctrl:1
	v_add_f32_dpp v40, v40, v40 quad_perm:[2,3,0,1] row_mask:0xf bank_mask:0xf bound_ctrl:1
	v_add_f32_dpp v54, v54, v54 quad_perm:[2,3,0,1] row_mask:0xf bank_mask:0xf bound_ctrl:1
	v_add_f32_e32 v4, v21, v4
	v_add_f32_dpp v55, v55, v55 quad_perm:[2,3,0,1] row_mask:0xf bank_mask:0xf bound_ctrl:1
	v_add_f32_e32 v40, v21, v40
	v_add_f32_e32 v54, v21, v54
	v_mul_f32_e32 v56, 0x3e4ccccd, v4
	v_add_f32_e32 v55, v21, v55
	v_mul_f32_e32 v57, 0x3e4ccccd, v40
	v_mul_f32_e32 v58, 0x3e4ccccd, v54
	v_max_f32_e32 v4, v4, v56
	v_mul_f32_e32 v59, 0x3e4ccccd, v55
	v_max_f32_e32 v40, v40, v57
	v_max_f32_e32 v54, v54, v58
	v_cndmask_b32_e64 v4, v37, v4, s[4:5]
	v_max_f32_e32 v55, v55, v59
	v_cndmask_b32_e64 v56, v37, v40, s[6:7]
	v_cndmask_b32_e64 v54, v37, v54, s[8:9]
	v_max_f32_e32 v40, 0xff800000, v4
	v_cndmask_b32_e64 v55, v37, v55, s[2:3]
	v_max3_f32 v40, v40, v56, v54
	v_max3_f32 v40, v39, v40, v55
	v_sub_f32_e32 v57, v39, v40
	v_sub_f32_e32 v4, v4, v40
	v_mul_f32_e32 v57, 0x3fb8aa3b, v57
	v_mul_f32_e32 v4, 0x3fb8aa3b, v4
	v_exp_f32_e32 v57, v57
	v_exp_f32_e32 v4, v4
	v_cmp_neq_f32_e64 s[10:11], v39, v40
	v_sub_f32_e32 v56, v56, v40
	v_sub_f32_e32 v54, v54, v40
	v_cndmask_b32_e64 v39, 1.0, v57, s[10:11]
	v_mul_f32_e32 v56, 0x3fb8aa3b, v56
	v_cndmask_b32_e64 v4, 0, v4, s[4:5]
	v_mul_f32_e32 v28, v39, v28
	v_mul_f32_e32 v27, v39, v27
	v_mul_f32_e32 v26, v39, v26
	v_mul_f32_e32 v25, v39, v25
	v_mul_f32_e32 v22, v39, v22
	v_mul_f32_e32 v20, v39, v20
	v_mul_f32_e32 v18, v39, v18
	v_mul_f32_e32 v15, v39, v15
	v_mul_f32_e32 v54, 0x3fb8aa3b, v54
	v_exp_f32_e32 v56, v56
	v_fma_mix_f32 v28, v42, v4, v28 op_sel:[0,0,0] op_sel_hi:[1,0,0]
	v_fma_mix_f32 v27, v42, v4, v27 op_sel:[1,0,0] op_sel_hi:[1,0,0]
	v_fma_mix_f32 v26, v43, v4, v26 op_sel:[0,0,0] op_sel_hi:[1,0,0]
	v_fma_mix_f32 v25, v43, v4, v25 op_sel:[1,0,0] op_sel_hi:[1,0,0]
	v_fma_mix_f32 v22, v44, v4, v22 op_sel:[0,0,0] op_sel_hi:[1,0,0]
	v_fma_mix_f32 v20, v44, v4, v20 op_sel:[1,0,0] op_sel_hi:[1,0,0]
	v_fma_mix_f32 v18, v45, v4, v18 op_sel:[0,0,0] op_sel_hi:[1,0,0]
	v_fma_mix_f32 v15, v45, v4, v15 op_sel:[1,0,0] op_sel_hi:[1,0,0]
	v_fmac_f32_e32 v4, v38, v39
	v_sub_f32_e32 v38, v55, v40
	v_exp_f32_e32 v54, v54
	v_mul_f32_e32 v38, 0x3fb8aa3b, v38
	v_exp_f32_e32 v38, v38
	v_cndmask_b32_e64 v56, 0, v56, s[6:7]
	v_cndmask_b32_e64 v54, 0, v54, s[8:9]
	v_fma_mix_f32 v28, v46, v56, v28 op_sel:[0,0,0] op_sel_hi:[1,0,0]
	v_fma_mix_f32 v27, v46, v56, v27 op_sel:[1,0,0] op_sel_hi:[1,0,0]
	v_fma_mix_f32 v26, v47, v56, v26 op_sel:[0,0,0] op_sel_hi:[1,0,0]
	v_fma_mix_f32 v25, v47, v56, v25 op_sel:[1,0,0] op_sel_hi:[1,0,0]
	v_fma_mix_f32 v22, v48, v56, v22 op_sel:[0,0,0] op_sel_hi:[1,0,0]
	v_fma_mix_f32 v20, v48, v56, v20 op_sel:[1,0,0] op_sel_hi:[1,0,0]
	v_fma_mix_f32 v18, v49, v56, v18 op_sel:[0,0,0] op_sel_hi:[1,0,0]
	v_fma_mix_f32 v15, v49, v56, v15 op_sel:[1,0,0] op_sel_hi:[1,0,0]
	v_add_f32_e32 v4, v4, v56
	v_fma_mix_f32 v28, v50, v54, v28 op_sel:[0,0,0] op_sel_hi:[1,0,0]
	v_fma_mix_f32 v27, v50, v54, v27 op_sel:[1,0,0] op_sel_hi:[1,0,0]
	v_fma_mix_f32 v26, v51, v54, v26 op_sel:[0,0,0] op_sel_hi:[1,0,0]
	v_fma_mix_f32 v25, v51, v54, v25 op_sel:[1,0,0] op_sel_hi:[1,0,0]
	v_fma_mix_f32 v22, v52, v54, v22 op_sel:[0,0,0] op_sel_hi:[1,0,0]
	v_fma_mix_f32 v20, v52, v54, v20 op_sel:[1,0,0] op_sel_hi:[1,0,0]
	v_fma_mix_f32 v18, v53, v54, v18 op_sel:[0,0,0] op_sel_hi:[1,0,0]
	v_fma_mix_f32 v15, v53, v54, v15 op_sel:[1,0,0] op_sel_hi:[1,0,0]
	v_add_f32_e32 v4, v4, v54
	v_cndmask_b32_e64 v38, 0, v38, s[2:3]
	v_cmp_ge_i32_e64 s[2:3], v24, v19
	v_fma_mix_f32 v28, v0, v38, v28 op_sel:[0,0,0] op_sel_hi:[1,0,0]
	v_fma_mix_f32 v27, v0, v38, v27 op_sel:[1,0,0] op_sel_hi:[1,0,0]
	v_fma_mix_f32 v26, v1, v38, v26 op_sel:[0,0,0] op_sel_hi:[1,0,0]
	v_fma_mix_f32 v25, v1, v38, v25 op_sel:[1,0,0] op_sel_hi:[1,0,0]
	v_fma_mix_f32 v22, v2, v38, v22 op_sel:[0,0,0] op_sel_hi:[1,0,0]
	v_fma_mix_f32 v20, v2, v38, v20 op_sel:[1,0,0] op_sel_hi:[1,0,0]
	v_fma_mix_f32 v18, v3, v38, v18 op_sel:[0,0,0] op_sel_hi:[1,0,0]
	v_fma_mix_f32 v15, v3, v38, v15 op_sel:[1,0,0] op_sel_hi:[1,0,0]
	v_add_f32_e32 v38, v4, v38
	s_or_b64 s[20:21], s[2:3], s[20:21]
	v_mov_b32_e32 v39, v40
	s_andn2_b64 exec, exec, s[20:21]
	s_cbranch_execz .LBB4_7
	.p2align	6
